# hd2: attention tile loops: the VALU of the first QK^T MFMA gap (2 v_exp + 3 v_add of the previous tile's tail) hoisted in front of the K-fragment wait; on top of cv1
# speedup vs baseline: 1.0026x; 1.0026x over previous
; __device__ __forceinline__ void qkt64c(f32x16& p0, f32x16& p1, const char* Ks, const bf16x8* qr, const f32x16& cinit, int r32, int hi) {
; #pragma unroll
;     for (int d0 = 0; d0 < 4; ++d0) { const int cb = (d0 * 16 + hi * 8) * 2;
;         const bf16x8 b0 = *reinterpret_cast<const bf16x8*>(Ks + kswz<64>(r32, cb));
;         const bf16x8 b1 = *reinterpret_cast<const bf16x8*>(Ks + kswz<64>(32 + r32, cb));
;         if (d0 == 0) { p0 = __builtin_amdgcn_mfma_f32_32x32x16_bf16(b0, qr[0], cinit, 0, 0, 0); p1 = __builtin_amdgcn_mfma_f32_32x32x16_bf16(b1, qr[0], cinit, 0, 0, 0); }
;         else { p0 = __builtin_amdgcn_mfma_f32_32x32x16_bf16(b0, qr[d0], p0, 0, 0, 0); p1 = __builtin_amdgcn_mfma_f32_32x32x16_bf16(b1, qr[d0], p1, 0, 0, 0); } }
; }
.Latt9_p1_top:
	ds_read_b128 v[144:147], v128 offset:49152
	ds_read_b128 v[148:151], v129 offset:49152
	ds_read_b128 v[152:155], v130 offset:49152
	ds_read_b128 v[156:159], v131 offset:49152
	ds_read_b128 v[232:235], v128 offset:53248
	ds_read_b128 v[236:239], v129 offset:53248
	ds_read_b128 v[240:243], v130 offset:53248
	ds_read_b128 v[244:247], v131 offset:53248
	s_lshl_b32 s19, s41, 14
	s_add_i32 s19, s19, s18
	s_mov_b32 m0, s19
	s_lshl_b32 s20, s41, 13
	global_load_lds_dwordx4 v195, s[16:17]
	s_add_i32 m0, s19, 0x2000
	s_add_i32 s20, s20, s18
	global_load_lds_dwordx4 v255, s[16:17]
	s_add_i32 m0, s20, 0xc000
	s_add_u32 s16, s16, 0x20000
	global_load_lds_dwordx4 v194, s[14:15]
	s_addc_u32 s17, s17, 0
	s_add_u32 s14, s14, 0x20000
	s_addc_u32 s15, s15, 0
	v_exp_f32_e32 v190, v120
	v_exp_f32_e32 v191, v121
	v_add_f32_e32 v120, v96, v97
	v_add_f32_e32 v121, v98, v99
	v_exp_f32_e32 v192, v122
	v_add_f32_e32 v120, v120, v121
	v_add_f32_e32 v121, v100, v101
	v_add_f32_e32 v122, v102, v103
	v_exp_f32_e32 v193, v123
	s_waitcnt lgkmcnt(7)
	v_mfma_f32_32x32x16_bf16 v[128:143], v[144:147], v[162:165], v[80:95]
	s_waitcnt lgkmcnt(6)
	v_mfma_f32_32x32x16_bf16 v[128:143], v[148:151], v[166:169], v[128:143]
	v_add_f32_e32 v121, v121, v122
	v_add_f32_e32 v122, v104, v105
	v_add_f32_e32 v123, v106, v107
	v_add_f32_e32 v122, v122, v123
	v_add_f32_e32 v123, v108, v109
	s_waitcnt lgkmcnt(5)
	v_mfma_f32_32x32x16_bf16 v[128:143], v[152:155], v[170:173], v[128:143]
	v_add_f32_e32 v208, v110, v111
	v_add_f32_e32 v123, v123, v208
	v_add_f32_e32 v208, v112, v113
	v_add_f32_e32 v209, v114, v115
	v_add_f32_e32 v208, v208, v209
	s_waitcnt lgkmcnt(4)
	v_mfma_f32_32x32x16_bf16 v[128:143], v[156:159], v[174:177], v[128:143]
	v_exp_f32_e32 v124, v124
	v_exp_f32_e32 v125, v125
	s_waitcnt lgkmcnt(3)
	v_mfma_f32_32x32x16_bf16 v[144:159], v[232:235], v[162:165], v[80:95]
	v_lshl_add_u32 v234, s12, 14, v217
	ds_read_b64_tr_b16 v[64:65], v234 offset:0
	ds_read_b64_tr_b16 v[66:67], v234 offset:0x800
	ds_read_b64_tr_b16 v[68:69], v234 offset:0x1000
	ds_read_b64_tr_b16 v[70:71], v234 offset:0x1800
	ds_read_b64_tr_b16 v[72:73], v234 offset:0x2000
	ds_read_b64_tr_b16 v[74:75], v234 offset:0x2800
	ds_read_b64_tr_b16 v[76:77], v234 offset:0x3000
	ds_read_b64_tr_b16 v[78:79], v234 offset:0x3800
	v_exp_f32_e32 v126, v126
	v_exp_f32_e32 v127, v127
	v_add_f32_e32 v120, v208, v120
	v_add_f32_e32 v208, v116, v117
	v_add_f32_e32 v209, v118, v119
	v_add_f32_e32 v208, v208, v209
	v_add_f32_e32 v121, v208, v121
	s_waitcnt lgkmcnt(10)
	v_mfma_f32_32x32x16_bf16 v[144:159], v[236:239], v[166:169], v[144:159]
	v_add_f32_e32 v208, v190, v191
	v_add_f32_e32 v209, v192, v193
	v_add_f32_e32 v208, v208, v209
	v_add_f32_e32 v122, v122, v208
	v_add_f32_e32 v208, v124, v125
	v_add_f32_e32 v209, v126, v127
	v_add_f32_e32 v208, v208, v209
	s_waitcnt lgkmcnt(9)
	v_mfma_f32_32x32x16_bf16 v[144:159], v[240:243], v[170:173], v[144:159]
	v_add_f32_e32 v123, v123, v208
	v_add_f32_e32 v120, v120, v121
	v_add_f32_e32 v121, v122, v123
	v_add_f32_e32 v231, v120, v121
	v_mov_b32_e32 v232, v231
	v_cvt_pk_bf16_f32 v96, v96, v97
	v_cvt_pk_bf16_f32 v97, v98, v99
	s_waitcnt lgkmcnt(8)
	v_mfma_f32_32x32x16_bf16 v[144:159], v[244:247], v[174:177], v[144:159]
	v_cvt_pk_bf16_f32 v98, v100, v101
	v_cvt_pk_bf16_f32 v99, v102, v103
	v_cvt_pk_bf16_f32 v120, v104, v105
	v_cvt_pk_bf16_f32 v121, v106, v107
	v_cvt_pk_bf16_f32 v122, v108, v109
	v_cvt_pk_bf16_f32 v123, v110, v111
	v_permlane32_swap_b32_e32 v96, v98
	v_permlane32_swap_b32_e32 v97, v99
	v_cvt_pk_bf16_f32 v104, v112, v113
	v_cvt_pk_bf16_f32 v105, v114, v115
	v_cvt_pk_bf16_f32 v106, v116, v117
	v_cvt_pk_bf16_f32 v107, v118, v119
	s_waitcnt lgkmcnt(0)
	v_mfma_f32_32x32x16_bf16 v[0:15], v[96:99], v[64:67], v[0:15]
	v_permlane32_swap_b32_e32 v120, v122
	v_permlane32_swap_b32_e32 v121, v123
	v_cvt_pk_bf16_f32 v100, v190, v191
	v_cvt_pk_bf16_f32 v101, v192, v193
	v_cvt_pk_bf16_f32 v102, v124, v125
	v_cvt_pk_bf16_f32 v103, v126, v127
	v_mfma_f32_32x32x16_bf16 v[0:15], v[120:123], v[68:71], v[0:15]
	v_permlane32_swap_b32_e32 v104, v106
	v_permlane32_swap_b32_e32 v105, v107
	ds_read_b64_tr_b16 v[236:237], v234 offset:0x200
	ds_read_b64_tr_b16 v[238:239], v234 offset:0xa00
	ds_read_b64_tr_b16 v[240:241], v234 offset:0x1200
	ds_read_b64_tr_b16 v[242:243], v234 offset:0x1a00
	ds_read_b64_tr_b16 v[244:245], v234 offset:0x2200
	ds_read_b64_tr_b16 v[246:247], v234 offset:0x2a00
	ds_read_b64_tr_b16 v[190:191], v234 offset:0x3200
	ds_read_b64_tr_b16 v[192:193], v234 offset:0x3a00
	v_mfma_f32_32x32x16_bf16 v[0:15], v[104:107], v[72:75], v[0:15]
	v_permlane32_swap_b32_e32 v100, v102
	v_permlane32_swap_b32_e32 v101, v103
	v_permlane32_swap_b32_e32 v231, v232
	v_max_f32_e32 v108, v128, v129
	v_max3_f32 v109, v130, v131, v145
	v_max3_f32 v108, v108, v144, v146
	v_max3_f32 v108, v108, v147, v132
	v_max3_f32 v109, v109, v134, v135
	v_mfma_f32_32x32x16_bf16 v[0:15], v[100:103], v[76:79], v[0:15]
	v_max3_f32 v208, v108, v133, v148
	v_max3_f32 v209, v109, v150, v151
	ds_read_b64_tr_b16 v[124:125], v234 offset:0x400
	ds_read_b64_tr_b16 v[126:127], v234 offset:0xc00
	ds_read_b64_tr_b16 v[116:117], v234 offset:0x1400
	ds_read_b64_tr_b16 v[118:119], v234 offset:0x1c00
	ds_read_b64_tr_b16 v[112:113], v234 offset:0x2400
	ds_read_b64_tr_b16 v[114:115], v234 offset:0x2c00
	ds_read_b64_tr_b16 v[108:109], v234 offset:0x3400
	ds_read_b64_tr_b16 v[110:111], v234 offset:0x3c00
	s_waitcnt lgkmcnt(8)
	v_mfma_f32_32x32x16_bf16 v[48:63], v[96:99], v[236:239], v[48:63]
	v_max3_f32 v208, v208, v149, v136
	v_max3_f32 v209, v209, v138, v139
	v_max3_f32 v208, v208, v137, v152
	v_max3_f32 v209, v209, v154, v155
	v_max3_f32 v208, v208, v153, v140
	v_max3_f32 v209, v209, v142, v143
	v_max3_f32 v208, v208, v141, v156
	v_mfma_f32_32x32x16_bf16 v[48:63], v[120:123], v[240:243], v[48:63]
	v_max3_f32 v209, v209, v158, v159
	v_max3_f32 v208, v208, v157, v209
	v_mov_b32_e32 v209, v208
	s_nop 1
	v_permlane32_swap_b32_e32 v208, v209
	v_mfma_f32_32x32x16_bf16 v[48:63], v[104:107], v[244:247], v[48:63]
	v_max_f32_e32 v233, v208, v209
	s_mov_b32 s2, 0x4138aa3b
	v_cmp_ge_f32_e32 vcc, s2, v233
	v_mfma_f32_32x32x16_bf16 v[48:63], v[100:103], v[190:193], v[48:63]
	s_cmp_eq_u64 vcc, exec
	s_cbranch_scc0 .LBB0_836
	v_mov_b32_e32 v233, 1.0

; __device__ __forceinline__ void qkt64c(f32x16& p0, f32x16& p1, const char* Ks, const bf16x8* qr, const f32x16& cinit, int r32, int hi) {
; #pragma unroll
;     for (int d0 = 0; d0 < 4; ++d0) { const int cb = (d0 * 16 + hi * 8) * 2;
;         const bf16x8 b0 = *reinterpret_cast<const bf16x8*>(Ks + kswz<64>(r32, cb));
;         const bf16x8 b1 = *reinterpret_cast<const bf16x8*>(Ks + kswz<64>(32 + r32, cb));
;         if (d0 == 0) { p0 = __builtin_amdgcn_mfma_f32_32x32x16_bf16(b0, qr[0], cinit, 0, 0, 0); p1 = __builtin_amdgcn_mfma_f32_32x32x16_bf16(b1, qr[0], cinit, 0, 0, 0); }
;         else { p0 = __builtin_amdgcn_mfma_f32_32x32x16_bf16(b0, qr[d0], p0, 0, 0, 0); p1 = __builtin_amdgcn_mfma_f32_32x32x16_bf16(b1, qr[d0], p1, 0, 0, 0); } }
; }
.LBB0_829:
	s_waitcnt lgkmcnt(0)
	v_add_u32_e32 v102, s2, v223
	v_add_u32_e32 v103, s2, v226
	v_add_u32_e32 v104, s2, v228
	v_add_u32_e32 v105, s2, v229
	s_waitcnt vmcnt(0)
	s_barrier
	ds_read_b128 v[112:115], v102 offset:49152
	ds_read_b128 v[116:119], v103 offset:49152
	ds_read_b128 v[120:123], v104 offset:49152
	ds_read_b128 v[124:127], v105 offset:49152
	ds_read_b128 v[190:193], v102 offset:53248
	ds_read_b128 v[202:205], v103 offset:53248
	ds_read_b128 v[234:237], v104 offset:53248
	ds_read_b128 v[238:241], v105 offset:53248
	s_add_i32 s3, s41, 1
	s_cmp_lg_u32 s41, 2
	s_cselect_b32 s3, s3, 0
	s_lshl_b32 s19, s3, 14
	s_add_i32 s19, s19, s18
	s_mov_b32 m0, s19
	s_lshl_b32 s20, s3, 13
	global_load_lds_dwordx4 v195, s[16:17]
	s_add_i32 m0, s19, 0x2000
	s_add_i32 s20, s20, s18
	global_load_lds_dwordx4 v255, s[16:17]
	s_add_i32 m0, s20, 0xc000
	s_add_u32 s16, s16, 0x20000
	global_load_lds_dwordx4 v194, s[14:15]
	s_addc_u32 s17, s17, 0
	s_add_u32 s14, s14, 0x20000
	s_addc_u32 s15, s15, 0
	v_exp_f32_e32 v208, v152
	v_exp_f32_e32 v209, v153
	v_add_f32_e32 v152, v128, v129
	v_add_f32_e32 v153, v130, v131
	v_exp_f32_e32 v210, v154
	v_add_f32_e32 v152, v152, v153
	v_add_f32_e32 v153, v132, v133
	v_add_f32_e32 v154, v134, v135
	v_exp_f32_e32 v211, v155
	s_waitcnt lgkmcnt(7)
	v_mfma_f32_32x32x16_bf16 v[96:111], v[112:115], v[162:165], v[80:95]
	s_waitcnt lgkmcnt(6)
	v_mfma_f32_32x32x16_bf16 v[96:111], v[116:119], v[166:169], v[96:111]
	v_add_f32_e32 v153, v153, v154
	v_add_f32_e32 v154, v136, v137
	v_add_f32_e32 v155, v138, v139
	v_add_f32_e32 v154, v154, v155
	v_add_f32_e32 v155, v140, v141
	s_waitcnt lgkmcnt(5)
	v_mfma_f32_32x32x16_bf16 v[96:111], v[120:123], v[170:173], v[96:111]
	v_exp_f32_e32 v156, v156
	v_exp_f32_e32 v157, v157
	v_exp_f32_e32 v158, v158
	v_exp_f32_e32 v159, v159
	s_waitcnt lgkmcnt(4)
	v_mfma_f32_32x32x16_bf16 v[96:111], v[124:127], v[174:177], v[96:111]
	s_waitcnt lgkmcnt(3)
	v_mfma_f32_32x32x16_bf16 v[112:127], v[190:193], v[162:165], v[80:95]
	v_add_f32_e32 v190, v142, v143
	v_add_f32_e32 v155, v155, v190
	v_add_f32_e32 v190, v144, v145
	v_add_f32_e32 v191, v146, v147
	v_add_f32_e32 v190, v190, v191
	v_add_f32_e32 v152, v152, v190
	v_add_f32_e32 v190, v148, v149
	s_waitcnt lgkmcnt(2)
	v_mfma_f32_32x32x16_bf16 v[112:127], v[202:205], v[166:169], v[112:127]
	v_lshl_add_u32 v205, s42, 14, v217
	ds_read_b64_tr_b16 v[64:65], v205 offset:0
	ds_read_b64_tr_b16 v[66:67], v205 offset:0x800
	ds_read_b64_tr_b16 v[68:69], v205 offset:0x1000
	ds_read_b64_tr_b16 v[70:71], v205 offset:0x1800
	ds_read_b64_tr_b16 v[72:73], v205 offset:0x2000
	ds_read_b64_tr_b16 v[74:75], v205 offset:0x2800
	ds_read_b64_tr_b16 v[76:77], v205 offset:0x3000
	ds_read_b64_tr_b16 v[78:79], v205 offset:0x3800
	v_add_f32_e32 v191, v150, v151
	v_add_f32_e32 v190, v190, v191
	v_add_f32_e32 v153, v153, v190
	v_add_f32_e32 v190, v208, v209
	v_add_f32_e32 v191, v210, v211
	v_add_f32_e32 v190, v190, v191
	v_add_f32_e32 v154, v154, v190
	s_waitcnt lgkmcnt(9)
	v_mfma_f32_32x32x16_bf16 v[112:127], v[234:237], v[170:173], v[112:127]
	v_add_f32_e32 v190, v156, v157
	v_add_f32_e32 v191, v158, v159
	v_add_f32_e32 v190, v190, v191
	v_add_f32_e32 v155, v155, v190
	v_add_f32_e32 v152, v152, v153
	v_add_f32_e32 v153, v154, v155
	v_add_f32_e32 v203, v152, v153
	s_waitcnt lgkmcnt(8)
	v_mfma_f32_32x32x16_bf16 v[112:127], v[238:241], v[174:177], v[112:127]
	v_mov_b32_e32 v204, v203
	v_cvt_pk_bf16_f32 v152, v128, v129
	v_cvt_pk_bf16_f32 v153, v130, v131
	v_cvt_pk_bf16_f32 v154, v132, v133
	v_cvt_pk_bf16_f32 v155, v134, v135
	v_cvt_pk_bf16_f32 v136, v136, v137
	v_cvt_pk_bf16_f32 v137, v138, v139
	v_cvt_pk_bf16_f32 v138, v140, v141
	v_cvt_pk_bf16_f32 v139, v142, v143
	v_permlane32_swap_b32_e32 v152, v154
	v_permlane32_swap_b32_e32 v153, v155
	v_cvt_pk_bf16_f32 v132, v144, v145
	v_cvt_pk_bf16_f32 v133, v146, v147
	v_cvt_pk_bf16_f32 v134, v148, v149
	v_cvt_pk_bf16_f32 v135, v150, v151
	s_waitcnt lgkmcnt(0)
	v_mfma_f32_32x32x16_bf16 v[0:15], v[152:155], v[64:67], v[0:15]
	v_permlane32_swap_b32_e32 v136, v138
	v_permlane32_swap_b32_e32 v137, v139
	v_cvt_pk_bf16_f32 v128, v208, v209
	v_cvt_pk_bf16_f32 v129, v210, v211
	v_cvt_pk_bf16_f32 v130, v156, v157
	v_cvt_pk_bf16_f32 v131, v158, v159
	v_mfma_f32_32x32x16_bf16 v[0:15], v[136:139], v[68:71], v[0:15]
	v_permlane32_swap_b32_e32 v132, v134
	v_permlane32_swap_b32_e32 v133, v135
	ds_read_b64_tr_b16 v[190:191], v205 offset:0x200
	ds_read_b64_tr_b16 v[192:193], v205 offset:0xa00
	ds_read_b64_tr_b16 v[234:235], v205 offset:0x1200
	ds_read_b64_tr_b16 v[236:237], v205 offset:0x1a00
	ds_read_b64_tr_b16 v[238:239], v205 offset:0x2200
	ds_read_b64_tr_b16 v[240:241], v205 offset:0x2a00
	ds_read_b64_tr_b16 v[242:243], v205 offset:0x3200
	ds_read_b64_tr_b16 v[244:245], v205 offset:0x3a00
	v_mfma_f32_32x32x16_bf16 v[0:15], v[132:135], v[72:75], v[0:15]
	v_permlane32_swap_b32_e32 v128, v130
	v_permlane32_swap_b32_e32 v129, v131
	v_permlane32_swap_b32_e32 v203, v204
	v_max_f32_e32 v140, v96, v97
	v_max3_f32 v140, v140, v112, v114
	v_max3_f32 v141, v98, v99, v113
	v_max3_f32 v140, v140, v115, v100
	v_max3_f32 v141, v141, v102, v103
	v_mfma_f32_32x32x16_bf16 v[0:15], v[128:131], v[76:79], v[0:15]
	v_max3_f32 v202, v140, v101, v116
	v_max3_f32 v208, v141, v118, v119
	ds_read_b64_tr_b16 v[156:157], v205 offset:0x400
	ds_read_b64_tr_b16 v[158:159], v205 offset:0xc00
	ds_read_b64_tr_b16 v[148:149], v205 offset:0x1400
	ds_read_b64_tr_b16 v[150:151], v205 offset:0x1c00
	ds_read_b64_tr_b16 v[144:145], v205 offset:0x2400
	ds_read_b64_tr_b16 v[146:147], v205 offset:0x2c00
	ds_read_b64_tr_b16 v[140:141], v205 offset:0x3400
	ds_read_b64_tr_b16 v[142:143], v205 offset:0x3c00
	s_waitcnt lgkmcnt(8)
	v_mfma_f32_32x32x16_bf16 v[48:63], v[152:155], v[190:193], v[48:63]
	v_max3_f32 v190, v202, v117, v104
	v_max3_f32 v191, v208, v106, v107
	v_max3_f32 v190, v190, v105, v120
	v_max3_f32 v191, v191, v122, v123
	v_max3_f32 v190, v190, v121, v108
	v_max3_f32 v191, v191, v110, v111
	v_max3_f32 v190, v190, v109, v124
	v_mfma_f32_32x32x16_bf16 v[48:63], v[136:139], v[234:237], v[48:63]
	v_max3_f32 v191, v191, v126, v127
	v_max3_f32 v190, v190, v125, v191
	v_mov_b32_e32 v191, v190
	s_nop 1
	v_permlane32_swap_b32_e32 v190, v191
	v_mfma_f32_32x32x16_bf16 v[48:63], v[132:135], v[238:241], v[48:63]
	v_max_f32_e32 v234, v190, v191
	s_mov_b32 s2, 0x4138aa3b
	v_cmp_ge_f32_e32 vcc, s2, v234
	v_mfma_f32_32x32x16_bf16 v[48:63], v[128:131], v[242:245], v[48:63]
	s_cmp_eq_u64 vcc, exec
	v_mov_b32_e32 v202, 1.0
	s_cbranch_scc0 .LBB0_837

; __device__ __forceinline__ void qkt64c(f32x16& p0, f32x16& p1, const char* Ks, const bf16x8* qr, const f32x16& cinit, int r32, int hi) {
; #pragma unroll
;     for (int d0 = 0; d0 < 4; ++d0) { const int cb = (d0 * 16 + hi * 8) * 2;
;         const bf16x8 b0 = *reinterpret_cast<const bf16x8*>(Ks + kswz<64>(r32, cb));
;         const bf16x8 b1 = *reinterpret_cast<const bf16x8*>(Ks + kswz<64>(32 + r32, cb));
;         if (d0 == 0) { p0 = __builtin_amdgcn_mfma_f32_32x32x16_bf16(b0, qr[0], cinit, 0, 0, 0); p1 = __builtin_amdgcn_mfma_f32_32x32x16_bf16(b1, qr[0], cinit, 0, 0, 0); }
;         else { p0 = __builtin_amdgcn_mfma_f32_32x32x16_bf16(b0, qr[d0], p0, 0, 0, 0); p1 = __builtin_amdgcn_mfma_f32_32x32x16_bf16(b1, qr[d0], p1, 0, 0, 0); } }
; }
.Latt9_p2_top:
	ds_read_b128 v[144:147], v128 offset:49152
	ds_read_b128 v[148:151], v129 offset:49152
	ds_read_b128 v[152:155], v130 offset:49152
	ds_read_b128 v[156:159], v131 offset:49152
	ds_read_b128 v[190:193], v128 offset:53248
	ds_read_b128 v[236:239], v129 offset:53248
	ds_read_b128 v[240:243], v130 offset:53248
	ds_read_b128 v[244:247], v131 offset:53248
	s_lshl_b32 s19, s29, 14
	s_add_i32 s19, s19, s18
	s_mov_b32 m0, s19
	s_lshl_b32 s20, s29, 13
	global_load_lds_dwordx4 v195, s[16:17]
	s_add_i32 m0, s19, 0x2000
	s_add_i32 s20, s20, s18
	global_load_lds_dwordx4 v255, s[16:17]
	s_add_i32 m0, s20, 0xc000
	s_add_u32 s16, s16, 0x20000
	global_load_lds_dwordx4 v194, s[14:15]
	s_addc_u32 s17, s17, 0
	s_add_u32 s14, s14, 0x20000
	s_addc_u32 s15, s15, 0
	v_exp_f32_e32 v208, v120
	v_exp_f32_e32 v209, v121
	v_add_f32_e32 v120, v96, v97
	v_add_f32_e32 v121, v98, v99
	v_exp_f32_e32 v210, v122
	v_add_f32_e32 v120, v120, v121
	v_add_f32_e32 v121, v100, v101
	v_add_f32_e32 v122, v102, v103
	v_exp_f32_e32 v211, v123
	s_waitcnt lgkmcnt(7)
	v_mfma_f32_32x32x16_bf16 v[128:143], v[144:147], v[162:165], v[80:95]
	s_waitcnt lgkmcnt(6)
	v_mfma_f32_32x32x16_bf16 v[128:143], v[148:151], v[166:169], v[128:143]
	v_add_f32_e32 v121, v121, v122
	v_add_f32_e32 v122, v104, v105
	v_add_f32_e32 v123, v106, v107
	v_add_f32_e32 v122, v122, v123
	v_add_f32_e32 v123, v108, v109
	s_waitcnt lgkmcnt(5)
	v_mfma_f32_32x32x16_bf16 v[128:143], v[152:155], v[170:173], v[128:143]
	v_exp_f32_e32 v124, v124
	v_exp_f32_e32 v125, v125
	v_exp_f32_e32 v126, v126
	v_exp_f32_e32 v127, v127
	v_cvt_pk_bf16_f32 v96, v96, v97
	s_waitcnt lgkmcnt(4)
	v_mfma_f32_32x32x16_bf16 v[128:143], v[156:159], v[174:177], v[128:143]
	v_cvt_pk_bf16_f32 v97, v98, v99
	v_cvt_pk_bf16_f32 v98, v100, v101
	v_cvt_pk_bf16_f32 v99, v102, v103
	s_nop 0
	v_permlane32_swap_b32_e32 v96, v98
	s_waitcnt lgkmcnt(3)
	v_mfma_f32_32x32x16_bf16 v[144:159], v[190:193], v[162:165], v[80:95]
	v_add_f32_e32 v190, v110, v111
	v_add_f32_e32 v123, v123, v190
	v_add_f32_e32 v190, v112, v113
	v_add_f32_e32 v191, v114, v115
	v_add_f32_e32 v190, v190, v191
	v_add_f32_e32 v120, v190, v120
	v_add_f32_e32 v190, v116, v117
	s_waitcnt lgkmcnt(2)
	v_mfma_f32_32x32x16_bf16 v[144:159], v[236:239], v[166:169], v[144:159]
	v_lshl_add_u32 v238, s12, 14, v221
	ds_read_b64_tr_b16 v[64:65], v238 offset:0
	ds_read_b64_tr_b16 v[66:67], v238 offset:0x800
	ds_read_b64_tr_b16 v[68:69], v238 offset:0x1000
	ds_read_b64_tr_b16 v[70:71], v238 offset:0x1800
	ds_read_b64_tr_b16 v[72:73], v238 offset:0x2000
	ds_read_b64_tr_b16 v[74:75], v238 offset:0x2800
	ds_read_b64_tr_b16 v[76:77], v238 offset:0x3000
	ds_read_b64_tr_b16 v[78:79], v238 offset:0x3800
	v_add_f32_e32 v191, v118, v119
	v_add_f32_e32 v190, v190, v191
	v_add_f32_e32 v121, v190, v121
	v_add_f32_e32 v190, v208, v209
	v_add_f32_e32 v191, v210, v211
	v_add_f32_e32 v190, v190, v191
	v_add_f32_e32 v122, v122, v190
	s_waitcnt lgkmcnt(9)
	v_mfma_f32_32x32x16_bf16 v[144:159], v[240:243], v[170:173], v[144:159]
	v_add_f32_e32 v190, v124, v125
	v_add_f32_e32 v191, v126, v127
	v_add_f32_e32 v190, v190, v191
	v_add_f32_e32 v123, v123, v190
	v_add_f32_e32 v120, v120, v121
	v_add_f32_e32 v121, v122, v123
	v_add_f32_e32 v235, v120, v121
	s_waitcnt lgkmcnt(8)
	v_mfma_f32_32x32x16_bf16 v[144:159], v[244:247], v[174:177], v[144:159]
	v_mov_b32_e32 v236, v235
	v_cvt_pk_bf16_f32 v120, v104, v105
	v_cvt_pk_bf16_f32 v121, v106, v107
	v_cvt_pk_bf16_f32 v122, v108, v109
	v_cvt_pk_bf16_f32 v123, v110, v111
	v_permlane32_swap_b32_e32 v97, v99
	v_cvt_pk_bf16_f32 v104, v112, v113
	v_cvt_pk_bf16_f32 v105, v114, v115
	v_cvt_pk_bf16_f32 v106, v116, v117
	v_cvt_pk_bf16_f32 v107, v118, v119
	s_waitcnt lgkmcnt(0)
	v_mfma_f32_32x32x16_bf16 v[0:15], v[96:99], v[64:67], v[0:15]
	v_permlane32_swap_b32_e32 v120, v122
	v_permlane32_swap_b32_e32 v121, v123
	v_cvt_pk_bf16_f32 v100, v208, v209
	v_cvt_pk_bf16_f32 v101, v210, v211
	v_cvt_pk_bf16_f32 v102, v124, v125
	v_cvt_pk_bf16_f32 v103, v126, v127
	v_mfma_f32_32x32x16_bf16 v[0:15], v[120:123], v[68:71], v[0:15]
	v_permlane32_swap_b32_e32 v104, v106
	v_permlane32_swap_b32_e32 v105, v107
	ds_read_b64_tr_b16 v[190:191], v238 offset:0x200
	ds_read_b64_tr_b16 v[192:193], v238 offset:0xa00
	ds_read_b64_tr_b16 v[240:241], v238 offset:0x1200
	ds_read_b64_tr_b16 v[242:243], v238 offset:0x1a00
	ds_read_b64_tr_b16 v[244:245], v238 offset:0x2200
	ds_read_b64_tr_b16 v[246:247], v238 offset:0x2a00
	ds_read_b64_tr_b16 v[208:209], v238 offset:0x3200
	ds_read_b64_tr_b16 v[210:211], v238 offset:0x3a00
	v_mfma_f32_32x32x16_bf16 v[0:15], v[104:107], v[72:75], v[0:15]
	v_permlane32_swap_b32_e32 v100, v102
	v_permlane32_swap_b32_e32 v101, v103
	v_permlane32_swap_b32_e32 v235, v236
	v_max_f32_e32 v108, v128, v129
	v_max3_f32 v108, v108, v144, v146
	v_max3_f32 v109, v130, v131, v145
	v_max3_f32 v108, v108, v147, v132
	v_max3_f32 v109, v109, v134, v135
	v_mfma_f32_32x32x16_bf16 v[0:15], v[100:103], v[76:79], v[0:15]
	v_max3_f32 v237, v108, v133, v148
	v_max3_f32 v239, v109, v150, v151
	ds_read_b64_tr_b16 v[124:125], v238 offset:0x400
	ds_read_b64_tr_b16 v[126:127], v238 offset:0xc00
	ds_read_b64_tr_b16 v[116:117], v238 offset:0x1400
	ds_read_b64_tr_b16 v[118:119], v238 offset:0x1c00
	ds_read_b64_tr_b16 v[112:113], v238 offset:0x2400
	ds_read_b64_tr_b16 v[114:115], v238 offset:0x2c00
	ds_read_b64_tr_b16 v[108:109], v238 offset:0x3400
	ds_read_b64_tr_b16 v[110:111], v238 offset:0x3c00
	s_waitcnt lgkmcnt(8)
	v_mfma_f32_32x32x16_bf16 v[48:63], v[96:99], v[190:193], v[48:63]
	v_max3_f32 v190, v237, v149, v136
	v_max3_f32 v191, v239, v138, v139
	v_max3_f32 v190, v190, v137, v152
	v_max3_f32 v191, v191, v154, v155
	v_max3_f32 v190, v190, v153, v140
	v_max3_f32 v191, v191, v142, v143
	v_max3_f32 v190, v190, v141, v156
	v_mfma_f32_32x32x16_bf16 v[48:63], v[120:123], v[240:243], v[48:63]
	v_max3_f32 v191, v191, v158, v159
	v_max3_f32 v190, v190, v157, v191
	v_mov_b32_e32 v191, v190
	s_nop 1
	v_permlane32_swap_b32_e32 v190, v191
	v_mfma_f32_32x32x16_bf16 v[48:63], v[104:107], v[244:247], v[48:63]
	v_max_f32_e32 v237, v190, v191
	s_mov_b32 s2, 0x4138aa3b
	v_cmp_ge_f32_e32 vcc, s2, v237
	v_mfma_f32_32x32x16_bf16 v[48:63], v[100:103], v[208:211], v[48:63]
	s_cmp_eq_u64 vcc, exec
	s_cbranch_scc0 .LBB0_859
	v_mov_b32_e32 v237, 1.0

; __device__ __forceinline__ void qkt64c(f32x16& p0, f32x16& p1, const char* Ks, const bf16x8* qr, const f32x16& cinit, int r32, int hi) {
; #pragma unroll
;     for (int d0 = 0; d0 < 4; ++d0) { const int cb = (d0 * 16 + hi * 8) * 2;
;         const bf16x8 b0 = *reinterpret_cast<const bf16x8*>(Ks + kswz<64>(r32, cb));
;         const bf16x8 b1 = *reinterpret_cast<const bf16x8*>(Ks + kswz<64>(32 + r32, cb));
;         if (d0 == 0) { p0 = __builtin_amdgcn_mfma_f32_32x32x16_bf16(b0, qr[0], cinit, 0, 0, 0); p1 = __builtin_amdgcn_mfma_f32_32x32x16_bf16(b1, qr[0], cinit, 0, 0, 0); }
;         else { p0 = __builtin_amdgcn_mfma_f32_32x32x16_bf16(b0, qr[d0], p0, 0, 0, 0); p1 = __builtin_amdgcn_mfma_f32_32x32x16_bf16(b1, qr[d0], p1, 0, 0, 0); } }
; }
.LBB0_852:
	s_waitcnt lgkmcnt(0)
	v_add_u32_e32 v102, s2, v227
	v_add_u32_e32 v103, s2, v231
	v_add_u32_e32 v104, s2, v232
	v_add_u32_e32 v105, s2, v233
	s_waitcnt vmcnt(0)
	s_barrier
	ds_read_b128 v[112:115], v102 offset:49152
	ds_read_b128 v[116:119], v103 offset:49152
	ds_read_b128 v[120:123], v104 offset:49152
	ds_read_b128 v[124:127], v105 offset:49152
	ds_read_b128 v[190:193], v102 offset:53248
	ds_read_b128 v[202:205], v103 offset:53248
	ds_read_b128 v[208:211], v104 offset:53248
	ds_read_b128 v[238:241], v105 offset:53248
	s_add_i32 s3, s29, 1
	s_cmp_lg_u32 s29, 2
	s_cselect_b32 s3, s3, 0
	s_lshl_b32 s19, s3, 14
	s_add_i32 s19, s19, s18
	s_mov_b32 m0, s19
	s_lshl_b32 s20, s3, 13
	global_load_lds_dwordx4 v195, s[16:17]
	s_add_i32 m0, s19, 0x2000
	s_add_i32 s20, s20, s18
	global_load_lds_dwordx4 v255, s[16:17]
	s_add_i32 m0, s20, 0xc000
	s_add_u32 s16, s16, 0x20000
	global_load_lds_dwordx4 v194, s[14:15]
	s_addc_u32 s17, s17, 0
	s_add_u32 s14, s14, 0x20000
	s_addc_u32 s15, s15, 0
	v_exp_f32_e32 v242, v152
	v_exp_f32_e32 v243, v153
	v_add_f32_e32 v152, v128, v129
	v_add_f32_e32 v153, v130, v131
	v_exp_f32_e32 v244, v154
	v_add_f32_e32 v152, v152, v153
	v_add_f32_e32 v153, v132, v133
	v_add_f32_e32 v154, v134, v135
	v_exp_f32_e32 v245, v155
	s_waitcnt lgkmcnt(7)
	v_mfma_f32_32x32x16_bf16 v[96:111], v[112:115], v[162:165], v[80:95]
	s_waitcnt lgkmcnt(6)
	v_mfma_f32_32x32x16_bf16 v[96:111], v[116:119], v[166:169], v[96:111]
	v_add_f32_e32 v153, v153, v154
	v_add_f32_e32 v154, v136, v137
	v_add_f32_e32 v155, v138, v139
	v_add_f32_e32 v154, v154, v155
	v_add_f32_e32 v155, v140, v141
	s_waitcnt lgkmcnt(5)
	v_mfma_f32_32x32x16_bf16 v[96:111], v[120:123], v[170:173], v[96:111]
	v_exp_f32_e32 v156, v156
	v_exp_f32_e32 v157, v157
	v_exp_f32_e32 v158, v158
	v_exp_f32_e32 v159, v159
	s_waitcnt lgkmcnt(4)
	v_mfma_f32_32x32x16_bf16 v[96:111], v[124:127], v[174:177], v[96:111]
	s_waitcnt lgkmcnt(3)
	v_mfma_f32_32x32x16_bf16 v[112:127], v[190:193], v[162:165], v[80:95]
	v_add_f32_e32 v190, v142, v143
	v_add_f32_e32 v155, v155, v190
	v_add_f32_e32 v190, v144, v145
	v_add_f32_e32 v191, v146, v147
	v_add_f32_e32 v190, v190, v191
	v_add_f32_e32 v152, v152, v190
	v_add_f32_e32 v190, v148, v149
	s_waitcnt lgkmcnt(2)
	v_mfma_f32_32x32x16_bf16 v[112:127], v[202:205], v[166:169], v[112:127]
	v_lshl_add_u32 v205, s30, 14, v221
	ds_read_b64_tr_b16 v[64:65], v205 offset:0
	ds_read_b64_tr_b16 v[66:67], v205 offset:0x800
	ds_read_b64_tr_b16 v[68:69], v205 offset:0x1000
	ds_read_b64_tr_b16 v[70:71], v205 offset:0x1800
	ds_read_b64_tr_b16 v[72:73], v205 offset:0x2000
	ds_read_b64_tr_b16 v[74:75], v205 offset:0x2800
	ds_read_b64_tr_b16 v[76:77], v205 offset:0x3000
	ds_read_b64_tr_b16 v[78:79], v205 offset:0x3800
	v_add_f32_e32 v191, v150, v151
	v_add_f32_e32 v190, v190, v191
	v_add_f32_e32 v153, v153, v190
	v_add_f32_e32 v190, v242, v243
	v_add_f32_e32 v191, v244, v245
	v_add_f32_e32 v190, v190, v191
	v_add_f32_e32 v154, v154, v190
	s_waitcnt lgkmcnt(9)
	v_mfma_f32_32x32x16_bf16 v[112:127], v[208:211], v[170:173], v[112:127]
	v_add_f32_e32 v190, v156, v157
	v_add_f32_e32 v191, v158, v159
	v_add_f32_e32 v190, v190, v191
	v_add_f32_e32 v155, v155, v190
	v_add_f32_e32 v152, v152, v153
	v_add_f32_e32 v153, v154, v155
	v_add_f32_e32 v203, v152, v153
	s_waitcnt lgkmcnt(8)
	v_mfma_f32_32x32x16_bf16 v[112:127], v[238:241], v[174:177], v[112:127]
	v_mov_b32_e32 v204, v203
	v_cvt_pk_bf16_f32 v152, v128, v129
	v_cvt_pk_bf16_f32 v153, v130, v131
	v_cvt_pk_bf16_f32 v154, v132, v133
	v_cvt_pk_bf16_f32 v155, v134, v135
	v_cvt_pk_bf16_f32 v136, v136, v137
	v_cvt_pk_bf16_f32 v137, v138, v139
	v_cvt_pk_bf16_f32 v138, v140, v141
	v_cvt_pk_bf16_f32 v139, v142, v143
	v_permlane32_swap_b32_e32 v152, v154
	v_permlane32_swap_b32_e32 v153, v155
	v_cvt_pk_bf16_f32 v132, v144, v145
	v_cvt_pk_bf16_f32 v133, v146, v147
	v_cvt_pk_bf16_f32 v134, v148, v149
	v_cvt_pk_bf16_f32 v135, v150, v151
	s_waitcnt lgkmcnt(0)
	v_mfma_f32_32x32x16_bf16 v[0:15], v[152:155], v[64:67], v[0:15]
	v_permlane32_swap_b32_e32 v136, v138
	v_permlane32_swap_b32_e32 v137, v139
	v_cvt_pk_bf16_f32 v128, v242, v243
	v_cvt_pk_bf16_f32 v129, v244, v245
	v_cvt_pk_bf16_f32 v130, v156, v157
	v_cvt_pk_bf16_f32 v131, v158, v159
	v_mfma_f32_32x32x16_bf16 v[0:15], v[136:139], v[68:71], v[0:15]
	v_permlane32_swap_b32_e32 v132, v134
	v_permlane32_swap_b32_e32 v133, v135
	ds_read_b64_tr_b16 v[190:191], v205 offset:0x200
	ds_read_b64_tr_b16 v[192:193], v205 offset:0xa00
	ds_read_b64_tr_b16 v[208:209], v205 offset:0x1200
	ds_read_b64_tr_b16 v[210:211], v205 offset:0x1a00
	ds_read_b64_tr_b16 v[238:239], v205 offset:0x2200
	ds_read_b64_tr_b16 v[240:241], v205 offset:0x2a00
	ds_read_b64_tr_b16 v[242:243], v205 offset:0x3200
	ds_read_b64_tr_b16 v[244:245], v205 offset:0x3a00
	v_mfma_f32_32x32x16_bf16 v[0:15], v[132:135], v[72:75], v[0:15]
	v_permlane32_swap_b32_e32 v128, v130
	v_permlane32_swap_b32_e32 v129, v131
	v_permlane32_swap_b32_e32 v203, v204
	v_max_f32_e32 v140, v96, v97
	v_max3_f32 v140, v140, v112, v114
	v_max3_f32 v141, v98, v99, v113
	v_max3_f32 v140, v140, v115, v100
	v_max3_f32 v141, v141, v102, v103
	v_mfma_f32_32x32x16_bf16 v[0:15], v[128:131], v[76:79], v[0:15]
	v_max3_f32 v202, v140, v101, v116
	v_max3_f32 v246, v141, v118, v119
	ds_read_b64_tr_b16 v[156:157], v205 offset:0x400
	ds_read_b64_tr_b16 v[158:159], v205 offset:0xc00
	ds_read_b64_tr_b16 v[148:149], v205 offset:0x1400
	ds_read_b64_tr_b16 v[150:151], v205 offset:0x1c00
	ds_read_b64_tr_b16 v[144:145], v205 offset:0x2400
	ds_read_b64_tr_b16 v[146:147], v205 offset:0x2c00
	ds_read_b64_tr_b16 v[140:141], v205 offset:0x3400
	ds_read_b64_tr_b16 v[142:143], v205 offset:0x3c00
	s_waitcnt lgkmcnt(8)
	v_mfma_f32_32x32x16_bf16 v[48:63], v[152:155], v[190:193], v[48:63]
	v_max3_f32 v190, v202, v117, v104
	v_max3_f32 v191, v246, v106, v107
	v_max3_f32 v190, v190, v105, v120
	v_max3_f32 v191, v191, v122, v123
	v_max3_f32 v190, v190, v121, v108
	v_max3_f32 v191, v191, v110, v111
	v_max3_f32 v190, v190, v109, v124
	v_mfma_f32_32x32x16_bf16 v[48:63], v[136:139], v[208:211], v[48:63]
	v_max3_f32 v191, v191, v126, v127
	v_max3_f32 v190, v190, v125, v191
	v_mov_b32_e32 v191, v190
	s_nop 1
	v_permlane32_swap_b32_e32 v190, v191
	v_mfma_f32_32x32x16_bf16 v[48:63], v[132:135], v[238:241], v[48:63]
	v_max_f32_e32 v238, v190, v191
	s_mov_b32 s2, 0x4138aa3b
	v_cmp_ge_f32_e32 vcc, s2, v238
	v_mfma_f32_32x32x16_bf16 v[48:63], v[128:131], v[242:245], v[48:63]
	s_cmp_eq_u64 vcc, exec
	v_mov_b32_e32 v202, 1.0
	s_cbranch_scc0 .LBB0_860
